# speedup vs baseline: 1.0019x; 1.0019x over previous
_Z5k_aggPKDF16_PKhPKiS4_PKDv8_DF16_PKfPDF16_Pf:
	s_load_dwordx8 s[4:11], s[0:1], 0x8
	s_load_dwordx4 s[12:15], s[0:1], 0x28
	s_load_dwordx2 s[16:17], s[0:1], 0x38
	v_lshlrev_b32_e32 v2, 4, v0
	s_lshl_b32 s0, s2, 2
	s_lshl_b32 s1, s2, 3
	s_andn2_b32 s0, s0, 63
	s_and_b32 s1, s1, 56
	s_or_b32 s0, s0, s1
	s_lshr_b32 s1, s2, 1
	s_and_b32 s1, s1, 4
	s_or_b32 s0, s0, s1
	v_lshlrev_b32_e32 v1, 2, v0
	v_lshrrev_b32_e32 v52, 6, v0
	v_or_b32_e32 v3, s0, v52
	v_mov_b32_e32 v98, v2
	s_waitcnt lgkmcnt(0)
	v_readfirstlane_b32 s19, v52
	s_nop 3
	s_lshl_b32 s19, s19, 10
	v_mov_b32_e32 v97, 0
	ds_write2st64_b32 v1, v97, v97 offset0:128 offset1:132
	ds_write2st64_b32 v1, v97, v97 offset0:136 offset1:140
	s_movk_i32 s0, 0x186a
	v_cmp_gt_i32_e32 vcc, s0, v3
	s_and_saveexec_b64 s[0:1], vcc
	s_cbranch_execz .Lagg_invalid
	v_bfe_u32 v4, v0, 2, 4
	v_lshlrev_b32_e32 v53, 4, v3
	v_or_b32_e32 v10, v53, v4
	v_and_b32_e32 v54, 48, v2
	v_lshl_or_b32 v11, v10, 7, v54
	global_load_dwordx4 v[2:5], v11, s[4:5]
	global_load_dwordx4 v[6:9], v11, s[4:5] offset:64
	v_ashrrev_i32_e32 v11, 31, v10
	v_lshl_add_u64 v[10:11], v[10:11], 2, s[6:7]
	global_load_dwordx2 v[50:51], v[10:11], off
	s_mov_b32 m0, s19
	s_nop 0
	global_load_lds_dwordx4 v98, s[10:11]
	s_add_u32 m0, s19, 0x1000
	v_add_u32_e32 v96, 0x1000, v98
	global_load_lds_dwordx4 v96, s[10:11]
	s_add_u32 m0, s19, 0x2000
	v_add_u32_e32 v96, 0x2000, v98
	global_load_lds_dwordx4 v96, s[10:11]
	s_add_u32 m0, s19, 0x3000
	v_add_u32_e32 v96, 0x3000, v98
	global_load_lds_dwordx4 v96, s[10:11]
	s_add_u32 m0, s19, 0x4000
	v_add_u32_e32 v96, 0x4000, v98
	global_load_lds_dwordx4 v96, s[10:11]
	s_add_u32 m0, s19, 0x5000
	v_add_u32_e32 v96, 0x5000, v98
	global_load_lds_dwordx4 v96, s[10:11]
	s_add_u32 m0, s19, 0x6000
	v_add_u32_e32 v96, 0x6000, v98
	global_load_lds_dwordx4 v96, s[10:11]
	s_add_u32 m0, s19, 0x7000
	v_add_u32_e32 v96, 0x7000, v98
	global_load_lds_dwordx4 v96, s[10:11]
	s_waitcnt vmcnt(10)
	v_cvt_pk_f32_fp8_e32 v[10:11], v2
	v_cvt_pk_f32_fp8_sdwa v[12:13], v2 src0_sel:WORD_1
	v_cvt_pk_f32_fp8_e32 v[14:15], v3
	v_cvt_pk_f32_fp8_sdwa v[2:3], v3 src0_sel:WORD_1
	v_cvt_pk_f32_fp8_e32 v[16:17], v4
	v_cvt_pk_f32_fp8_sdwa v[18:19], v4 src0_sel:WORD_1
	v_cvt_pk_f32_fp8_e32 v[20:21], v5
	v_cvt_pk_f32_fp8_sdwa v[4:5], v5 src0_sel:WORD_1
	s_waitcnt vmcnt(9)
	v_cvt_pk_f32_fp8_e32 v[22:23], v6
	v_cvt_pk_f32_fp8_sdwa v[24:25], v6 src0_sel:WORD_1
	v_cvt_pk_f32_fp8_e32 v[26:27], v7
	v_cvt_pk_f32_fp8_sdwa v[6:7], v7 src0_sel:WORD_1
	v_cvt_pk_f32_fp8_e32 v[28:29], v8
	v_cvt_pk_f32_fp8_sdwa v[30:31], v8 src0_sel:WORD_1
	v_cvt_pk_f32_fp8_e32 v[32:33], v9
	v_cvt_pk_f32_fp8_sdwa v[8:9], v9 src0_sel:WORD_1
	v_add_f32_e32 v88, 0, v10
	v_add_f32_e32 v89, 0, v11
	v_add_f32_e32 v90, 0, v12
	v_add_f32_e32 v91, 0, v13
	v_add_f32_e32 v92, 0, v14
	v_add_f32_e32 v93, 0, v15
	v_add_f32_e32 v94, 0, v2
	v_add_f32_e32 v95, 0, v3
	v_add_f32_e32 v76, 0, v16
	v_add_f32_e32 v77, 0, v17
	v_add_f32_e32 v80, 0, v18
	v_add_f32_e32 v81, 0, v19
	v_add_f32_e32 v84, 0, v20
	v_add_f32_e32 v85, 0, v21
	v_add_f32_e32 v86, 0, v4
	v_add_f32_e32 v87, 0, v5
	v_add_f32_e32 v72, 0, v22
	v_add_f32_e32 v73, 0, v23
	v_add_f32_e32 v74, 0, v24
	v_add_f32_e32 v75, 0, v25
	v_add_f32_e32 v78, 0, v26
	v_add_f32_e32 v79, 0, v27
	v_add_f32_e32 v82, 0, v6
	v_add_f32_e32 v83, 0, v7
	v_add_f32_e32 v64, 0, v28
	v_add_f32_e32 v65, 0, v29
	v_add_f32_e32 v66, 0, v30
	v_add_f32_e32 v67, 0, v31
	v_add_f32_e32 v68, 0, v32
	v_add_f32_e32 v69, 0, v33
	v_add_f32_e32 v70, 0, v8
	v_add_f32_e32 v71, 0, v9
	s_waitcnt vmcnt(8)
	s_mov_b64 s[6:7], exec
	v_mov_b32_e32 v63, 0xc35000
	v_add_u32_e32 v106, 0, v50
	v_lshlrev_b32_e32 v106, 2, v106
	global_load_dwordx3 v[56:58], v106, s[8:9]
	v_add_u32_e32 v106, 3, v50
	v_lshlrev_b32_e32 v106, 2, v106
	global_load_dwordx3 v[60:62], v106, s[8:9]
	s_waitcnt vmcnt(0)
	v_add_u32_e32 v104, 0, v50
	v_cmp_lt_i32_e32 vcc, v104, v51
	v_lshlrev_b32_e32 v105, 7, v56
	s_nop 0
	v_cndmask_b32_e32 v105, v63, v105, vcc
	v_or_b32_e32 v105, v54, v105
	global_load_dwordx4 v[2:5], v105, s[4:5]
	global_load_dwordx4 v[6:9], v105, s[4:5] offset:64
	v_add_u32_e32 v104, 1, v50
	v_cmp_lt_i32_e32 vcc, v104, v51
	v_lshlrev_b32_e32 v105, 7, v57
	s_nop 0
	v_cndmask_b32_e32 v105, v63, v105, vcc
	v_or_b32_e32 v105, v54, v105
	global_load_dwordx4 v[10:13], v105, s[4:5]
	global_load_dwordx4 v[14:17], v105, s[4:5] offset:64
	v_add_u32_e32 v104, 2, v50
	v_cmp_lt_i32_e32 vcc, v104, v51
	v_lshlrev_b32_e32 v105, 7, v58
	s_nop 0
	v_cndmask_b32_e32 v105, v63, v105, vcc
	v_or_b32_e32 v105, v54, v105
	global_load_dwordx4 v[18:21], v105, s[4:5]
	global_load_dwordx4 v[22:25], v105, s[4:5] offset:64
	v_add_u32_e32 v106, 6, v50
	v_lshlrev_b32_e32 v106, 2, v106
	global_load_dwordx3 v[56:58], v106, s[8:9]
	v_add_u32_e32 v104, 3, v50
	v_cmp_lt_i32_e32 vcc, v104, v51
	v_lshlrev_b32_e32 v105, 7, v60
	s_nop 0
	v_cndmask_b32_e32 v105, v63, v105, vcc
	v_or_b32_e32 v105, v54, v105
	global_load_dwordx4 v[26:29], v105, s[4:5]
	global_load_dwordx4 v[30:33], v105, s[4:5] offset:64
	v_add_u32_e32 v104, 4, v50
	v_cmp_lt_i32_e32 vcc, v104, v51
	v_lshlrev_b32_e32 v105, 7, v61
	s_nop 0
	v_cndmask_b32_e32 v105, v63, v105, vcc
	v_or_b32_e32 v105, v54, v105
	global_load_dwordx4 v[34:37], v105, s[4:5]
	global_load_dwordx4 v[38:41], v105, s[4:5] offset:64
	v_add_u32_e32 v104, 5, v50
	v_cmp_lt_i32_e32 vcc, v104, v51
	v_lshlrev_b32_e32 v105, 7, v62
	s_nop 0
	v_cndmask_b32_e32 v105, v63, v105, vcc
	v_or_b32_e32 v105, v54, v105
	global_load_dwordx4 v[42:45], v105, s[4:5]
	global_load_dwordx4 v[46:49], v105, s[4:5] offset:64
	v_add_u32_e32 v106, 9, v50
	v_lshlrev_b32_e32 v106, 2, v106
	global_load_dwordx3 v[60:62], v106, s[8:9]

.Lagg_invalid:
	s_or_b64 exec, exec, s[0:1]
	s_mov_b32 m0, s19
	s_nop 0
	global_load_lds_dwordx4 v98, s[10:11]
	s_add_u32 m0, s19, 0x1000
	v_add_u32_e32 v96, 0x1000, v98
	global_load_lds_dwordx4 v96, s[10:11]
	s_add_u32 m0, s19, 0x2000
	v_add_u32_e32 v96, 0x2000, v98
	global_load_lds_dwordx4 v96, s[10:11]
	s_add_u32 m0, s19, 0x3000
	v_add_u32_e32 v96, 0x3000, v98
	global_load_lds_dwordx4 v96, s[10:11]
	s_add_u32 m0, s19, 0x4000
	v_add_u32_e32 v96, 0x4000, v98
	global_load_lds_dwordx4 v96, s[10:11]
	s_add_u32 m0, s19, 0x5000
	v_add_u32_e32 v96, 0x5000, v98
	global_load_lds_dwordx4 v96, s[10:11]
	s_add_u32 m0, s19, 0x6000
	v_add_u32_e32 v96, 0x6000, v98
	global_load_lds_dwordx4 v96, s[10:11]
	s_add_u32 m0, s19, 0x7000
	v_add_u32_e32 v96, 0x7000, v98
	global_load_lds_dwordx4 v96, s[10:11]
	s_waitcnt vmcnt(0)
	s_waitcnt lgkmcnt(0)
	s_barrier
	s_branch .LBB2_8
